# v34 + dead bias-address VALU/SALU (left over from the LDS bias prefetch) removed after the gate/up K-loop
# baseline (speedup 1.0000x reference)
.LBB0_249:
	s_add_u32 s4, s46, s26
	s_addc_u32 s36, s47, s27
	s_add_u32 s69, s4, 0x2e000100
	s_addc_u32 s70, s36, 0
	s_add_u32 s74, s61, s26
	s_addc_u32 s86, s63, s27
	s_add_i32 s4, 0, 0x10000
	s_cmpk_eq_i32 s26, 0x300
	s_cselect_b64 vcc, -1, 0
	s_and_b64 s[36:37], vcc, exec
	s_cselect_b32 s71, s41, s70
	s_cselect_b32 s70, s40, s69
	v_add_u32_e32 v0, s4, v200
	s_cselect_b32 s37, s6, s86
	s_cselect_b32 s36, s31, s74
	s_add_i32 s69, 0, 0x14000
	ds_read_b128 v[18:21], v0
	ds_read_b128 v[22:25], v0 offset:1024
	ds_read_b128 v[26:29], v0 offset:2048
	ds_read_b128 v[30:33], v0 offset:3072
	v_add_u32_e32 v0, s69, v200
	ds_read_b128 v[2:5], v0
	ds_read_b128 v[6:9], v0 offset:1024
	ds_read_b128 v[10:13], v0 offset:2048
	ds_read_b128 v[14:17], v0 offset:3072
	v_lshl_add_u64 v[222:223], v[178:179], 0, s[26:27]
	s_add_i32 m0, s93, 0xc000
	ds_read_b128 v[180:183], v201
	ds_read_b128 v[184:187], v201 offset:1024
	ds_read_b128 v[206:209], v201 offset:2048
	ds_read_b128 v[210:213], v201 offset:3072
	ds_read_b128 v[214:217], v201 offset:4096
	ds_read_b128 v[218:221], v201 offset:5120
	ds_read_b128 v[234:237], v201 offset:6144
	ds_read_b128 v[238:241], v201 offset:7168
	global_load_lds_dwordx4 v[222:223], off
	v_lshl_add_u64 v[222:223], v[176:177], 0, s[26:27]
	s_add_i32 m0, s93, 0xe000
	s_nop 0
	global_load_lds_dwordx4 v[222:223], off
	s_waitcnt vmcnt(8)
	s_waitcnt lgkmcnt(0)
	s_barrier
	s_setprio 1
	s_waitcnt lgkmcnt(0)
	v_mfma_f32_16x16x128_f8f6f4 v[158:161], v[18:25], v[180:187], v[158:161]
	v_mfma_f32_16x16x128_f8f6f4 v[154:157], v[26:33], v[180:187], v[154:157]
	v_mfma_f32_16x16x128_f8f6f4 v[142:145], v[18:25], v[206:213], v[142:145]
	v_mfma_f32_16x16x128_f8f6f4 v[138:141], v[26:33], v[206:213], v[138:141]
	v_mfma_f32_16x16x128_f8f6f4 v[126:129], v[18:25], v[214:221], v[126:129]
	v_mfma_f32_16x16x128_f8f6f4 v[122:125], v[26:33], v[214:221], v[122:125]
	v_mfma_f32_16x16x128_f8f6f4 v[110:113], v[18:25], v[234:241], v[110:113]
	v_mfma_f32_16x16x128_f8f6f4 v[106:109], v[26:33], v[234:241], v[106:109]
	s_setprio 0
	s_setprio 1
	v_mfma_f32_16x16x128_f8f6f4 v[150:153], v[2:9], v[180:187], v[150:153]
	v_mfma_f32_16x16x128_f8f6f4 v[146:149], v[10:17], v[180:187], v[146:149]
	v_mfma_f32_16x16x128_f8f6f4 v[134:137], v[2:9], v[206:213], v[134:137]
	v_mfma_f32_16x16x128_f8f6f4 v[130:133], v[10:17], v[206:213], v[130:133]
	v_mfma_f32_16x16x128_f8f6f4 v[118:121], v[2:9], v[214:221], v[118:121]
	v_mfma_f32_16x16x128_f8f6f4 v[114:117], v[10:17], v[214:221], v[114:117]
	v_mfma_f32_16x16x128_f8f6f4 v[102:105], v[2:9], v[234:241], v[102:105]
	v_mfma_f32_16x16x128_f8f6f4 v[98:101], v[10:17], v[234:241], v[98:101]
	s_setprio 0
	s_barrier
	s_add_i32 s4, s4, s92
	v_lshl_add_u64 v[180:181], s[36:37], 0, v[162:163]
	s_mov_b32 m0, s4
	ds_read_b128 v[206:209], v201 offset:16384
	ds_read_b128 v[210:213], v201 offset:17408
	ds_read_b128 v[214:217], v201 offset:18432
	ds_read_b128 v[218:221], v201 offset:19456
	ds_read_b128 v[234:237], v201 offset:20480
	ds_read_b128 v[238:241], v201 offset:21504
	ds_read_b128 v[242:245], v201 offset:22528
	ds_read_b128 v[246:249], v201 offset:23552
	global_load_lds_dwordx4 v[180:181], off
	s_add_i32 m0, s4, 0x2000
	s_add_u32 s86, s36, 0x20000
	v_lshl_add_u64 v[182:183], s[36:37], 0, v[164:165]
	s_addc_u32 s87, s37, 0
	s_add_i32 s4, s69, s92
	global_load_lds_dwordx4 v[182:183], off
	v_lshl_add_u64 v[184:185], s[86:87], 0, v[162:163]
	s_mov_b32 m0, s4
	v_cndmask_b32_e32 v0, v168, v202, vcc
	global_load_lds_dwordx4 v[184:185], off
	v_lshl_add_u64 v[184:185], s[86:87], 0, v[164:165]
	s_add_i32 m0, s4, 0x2000
	v_lshl_add_u64 v[186:187], s[70:71], 0, v[0:1]
	global_load_lds_dwordx4 v[184:185], off
	s_mov_b32 m0, s93
	v_cndmask_b32_e32 v184, v170, v203, vcc
	global_load_lds_dwordx4 v0, s[70:71]
	s_mov_b32 m0, s79
	v_mov_b32_e32 v185, v1
	global_load_lds_dwordx4 v184, s[70:71]
	s_waitcnt vmcnt(8)
	s_waitcnt lgkmcnt(0)
	v_lshl_add_u64 v[184:185], s[70:71], 0, v[184:185]
	s_barrier
	s_setprio 1
	s_waitcnt lgkmcnt(0)
	v_mfma_f32_16x16x128_f8f6f4 v[94:97], v[18:25], v[206:213], v[94:97]
	v_mfma_f32_16x16x128_f8f6f4 v[90:93], v[26:33], v[206:213], v[90:93]
	v_mfma_f32_16x16x128_f8f6f4 v[70:73], v[18:25], v[214:221], v[70:73]
	v_mfma_f32_16x16x128_f8f6f4 v[66:69], v[26:33], v[214:221], v[66:69]
	v_mfma_f32_16x16x128_f8f6f4 v[54:57], v[18:25], v[234:241], v[54:57]
	v_mfma_f32_16x16x128_f8f6f4 v[50:53], v[26:33], v[234:241], v[50:53]
	v_mfma_f32_16x16x128_f8f6f4 v[38:41], v[18:25], v[242:249], v[38:41]
	v_mfma_f32_16x16x128_f8f6f4 v[34:37], v[26:33], v[242:249], v[34:37]
	s_setprio 0
	s_setprio 1
	v_mfma_f32_16x16x128_f8f6f4 v[86:89], v[2:9], v[206:213], v[86:89]
	v_mfma_f32_16x16x128_f8f6f4 v[82:85], v[10:17], v[206:213], v[82:85]
	v_mfma_f32_16x16x128_f8f6f4 v[78:81], v[2:9], v[214:221], v[78:81]
	v_mfma_f32_16x16x128_f8f6f4 v[74:77], v[10:17], v[214:221], v[74:77]
	v_mfma_f32_16x16x128_f8f6f4 v[62:65], v[2:9], v[234:241], v[62:65]
	v_mfma_f32_16x16x128_f8f6f4 v[58:61], v[10:17], v[234:241], v[58:61]
	v_mfma_f32_16x16x128_f8f6f4 v[46:49], v[2:9], v[242:249], v[46:49]
	v_mfma_f32_16x16x128_f8f6f4 v[42:45], v[10:17], v[242:249], v[42:45]
	s_setprio 0
	s_barrier
	s_add_i32 s4, 0, 0x18000
	v_add_u32_e32 v0, s4, v200
	s_add_i32 s69, 0, 0x1c000
	ds_read_b128 v[2:5], v0
	ds_read_b128 v[6:9], v0 offset:1024
	ds_read_b128 v[10:13], v0 offset:2048
	ds_read_b128 v[14:17], v0 offset:3072
	v_add_u32_e32 v0, s69, v200
	ds_read_b128 v[18:21], v0
	ds_read_b128 v[22:25], v0 offset:1024
	ds_read_b128 v[26:29], v0 offset:2048
	ds_read_b128 v[30:33], v0 offset:3072
	s_mov_b32 m0, s84
	v_cndmask_b32_e32 v0, v172, v204, vcc
	ds_read_b128 v[206:209], v201 offset:32768
	ds_read_b128 v[210:213], v201 offset:33792
	ds_read_b128 v[214:217], v201 offset:34816
	ds_read_b128 v[218:221], v201 offset:35840
	ds_read_b128 v[234:237], v201 offset:36864
	ds_read_b128 v[238:241], v201 offset:37888
	ds_read_b128 v[242:245], v201 offset:38912
	ds_read_b128 v[246:249], v201 offset:39936
	v_cndmask_b32_e32 v173, v174, v205, vcc
	global_load_lds_dwordx4 v0, s[70:71]
	s_mov_b32 m0, s85
	s_nop 0
	global_load_lds_dwordx4 v173, s[70:71]
	s_waitcnt vmcnt(8)
	s_waitcnt lgkmcnt(0)
	s_barrier
	s_setprio 1
	s_waitcnt lgkmcnt(0)
	v_mfma_f32_16x16x128_f8f6f4 v[158:161], v[2:9], v[206:213], v[158:161]
	v_mfma_f32_16x16x128_f8f6f4 v[154:157], v[10:17], v[206:213], v[154:157]
	v_mfma_f32_16x16x128_f8f6f4 v[142:145], v[2:9], v[214:221], v[142:145]
	v_mfma_f32_16x16x128_f8f6f4 v[138:141], v[10:17], v[214:221], v[138:141]
	v_mfma_f32_16x16x128_f8f6f4 v[126:129], v[2:9], v[234:241], v[126:129]
	v_mfma_f32_16x16x128_f8f6f4 v[122:125], v[10:17], v[234:241], v[122:125]
	v_mfma_f32_16x16x128_f8f6f4 v[110:113], v[2:9], v[242:249], v[110:113]
	v_mfma_f32_16x16x128_f8f6f4 v[106:109], v[10:17], v[242:249], v[106:109]
	s_setprio 0
	s_setprio 1
	v_mfma_f32_16x16x128_f8f6f4 v[150:153], v[18:25], v[206:213], v[150:153]
	v_mfma_f32_16x16x128_f8f6f4 v[146:149], v[26:33], v[206:213], v[146:149]
	v_mfma_f32_16x16x128_f8f6f4 v[134:137], v[18:25], v[214:221], v[134:137]
	v_mfma_f32_16x16x128_f8f6f4 v[130:133], v[26:33], v[214:221], v[130:133]
	v_mfma_f32_16x16x128_f8f6f4 v[118:121], v[18:25], v[234:241], v[118:121]
	v_mfma_f32_16x16x128_f8f6f4 v[114:117], v[26:33], v[234:241], v[114:117]
	v_mfma_f32_16x16x128_f8f6f4 v[102:105], v[18:25], v[242:249], v[102:105]
	v_mfma_f32_16x16x128_f8f6f4 v[98:101], v[26:33], v[242:249], v[98:101]
	s_setprio 0
	s_barrier
	s_add_i32 s4, s4, s92
	v_lshl_add_u64 v[180:181], v[180:181], 0, s[22:23]
	s_mov_b32 m0, s4
	ds_read_b128 v[206:209], v201 offset:49152
	ds_read_b128 v[210:213], v201 offset:50176
	ds_read_b128 v[214:217], v201 offset:51200
	ds_read_b128 v[218:221], v201 offset:52224
	ds_read_b128 v[234:237], v201 offset:53248
	ds_read_b128 v[238:241], v201 offset:54272
	ds_read_b128 v[242:245], v201 offset:55296
	ds_read_b128 v[246:249], v201 offset:56320
	global_load_lds_dwordx4 v[180:181], off
	s_add_i32 m0, s4, 0x2000
	s_add_u32 s36, s36, 0x20080
	v_lshl_add_u64 v[180:181], v[182:183], 0, s[22:23]
	s_addc_u32 s37, s37, 0
	s_add_i32 s4, s69, s92
	global_load_lds_dwordx4 v[180:181], off
	v_lshl_add_u64 v[180:181], s[36:37], 0, v[162:163]
	s_mov_b32 m0, s4
	s_nop 0
	global_load_lds_dwordx4 v[180:181], off
	v_lshl_add_u64 v[180:181], s[36:37], 0, v[164:165]
	s_add_i32 m0, s4, 0x2000
	s_nop 0
	global_load_lds_dwordx4 v[180:181], off
	v_lshl_add_u64 v[180:181], v[186:187], 0, s[22:23]
	s_mov_b32 m0, s15
	s_nop 0
	global_load_lds_dwordx4 v[180:181], off
	v_lshl_add_u64 v[180:181], v[184:185], 0, s[22:23]
	s_mov_b32 m0, s16
	s_nop 0
	global_load_lds_dwordx4 v[180:181], off
	s_waitcnt vmcnt(8)
	s_waitcnt lgkmcnt(0)
	s_barrier
	s_setprio 1
	s_waitcnt lgkmcnt(0)
	v_mfma_f32_16x16x128_f8f6f4 v[94:97], v[2:9], v[206:213], v[94:97]
	v_mfma_f32_16x16x128_f8f6f4 v[90:93], v[10:17], v[206:213], v[90:93]
	v_mfma_f32_16x16x128_f8f6f4 v[70:73], v[2:9], v[214:221], v[70:73]
	v_mfma_f32_16x16x128_f8f6f4 v[66:69], v[10:17], v[214:221], v[66:69]
	v_mfma_f32_16x16x128_f8f6f4 v[54:57], v[2:9], v[234:241], v[54:57]
	v_mfma_f32_16x16x128_f8f6f4 v[50:53], v[10:17], v[234:241], v[50:53]
	v_mfma_f32_16x16x128_f8f6f4 v[38:41], v[2:9], v[242:249], v[38:41]
	v_mfma_f32_16x16x128_f8f6f4 v[34:37], v[10:17], v[242:249], v[34:37]
	s_setprio 0
	s_setprio 1
	v_mfma_f32_16x16x128_f8f6f4 v[86:89], v[18:25], v[206:213], v[86:89]
	v_mfma_f32_16x16x128_f8f6f4 v[82:85], v[26:33], v[206:213], v[82:85]
	v_mfma_f32_16x16x128_f8f6f4 v[78:81], v[18:25], v[214:221], v[78:81]
	v_mfma_f32_16x16x128_f8f6f4 v[74:77], v[26:33], v[214:221], v[74:77]
	v_mfma_f32_16x16x128_f8f6f4 v[62:65], v[18:25], v[234:241], v[62:65]
	v_mfma_f32_16x16x128_f8f6f4 v[58:61], v[26:33], v[234:241], v[58:61]
	v_mfma_f32_16x16x128_f8f6f4 v[46:49], v[18:25], v[242:249], v[46:49]
	v_mfma_f32_16x16x128_f8f6f4 v[42:45], v[26:33], v[242:249], v[42:45]
	s_setprio 0
	s_barrier
	s_add_i32 s67, s67, 2
	s_add_u32 s26, s26, 0x100
	s_addc_u32 s27, s27, 0
	s_cmp_gt_u32 s67, 5
	s_cbranch_scc0 .LBB0_249
	s_lshl_b32 s66, s66, 7
	ds_read_b128 v[2:5], v233 offset:64
	ds_read_b128 v[10:13], v233
	v_lshl_add_u32 v22, s75, 8, v171
	ds_read_b128 v[6:9], v233 offset:128
	ds_read_b128 v[14:17], v233 offset:192
	s_and_b64 vcc, exec, s[58:59]
	s_cbranch_vccz .LBB0_252
	s_barrier
